# speedup vs baseline: 1.0134x; 1.0005x over previous
_Z10qkv_kernelPKfS0_S0_PKdPKtS0_PhPfS6_:
	s_bfe_u32 s30, s2, 0x20001
	s_and_b32 s31, s2, 1
	s_lshr_b32 s2, s2, 3
	s_lshl_b32 s30, s30, 6
	s_lshl_b32 s31, s31, 5
	s_or_b32 s2, s2, s30
	s_or_b32 s2, s2, s31
	s_load_dwordx2 s[8:9], s[0:1], 0x0
	s_load_dwordx4 s[4:7], s[0:1], 0x18
	s_load_dwordx4 s[20:23], s[0:1], 0x8
	s_load_dwordx2 s[30:31], s[0:1], 0x28
	v_lshrrev_b32_e32 v1, 6, v0
	v_and_b32_e32 v146, 63, v0
	v_lshlrev_b32_e32 v134, 14, v1
	v_mov_b32_e32 v135, 0
	s_waitcnt lgkmcnt(0)
	v_lshrrev_b32_e32 v188, 6, v0
	v_and_b32_e32 v189, 31, v0
	v_lshl_add_u32 v188, v188, 5, v189
	v_lshlrev_b32_e32 v188, 2, v188
	global_load_dword v190, v188, s[20:21]
	global_load_dword v191, v188, s[22:23]
	v_lshl_add_u64 v[2:3], s[6:7], 0, v[134:135]
	v_lshlrev_b32_e32 v134, 4, v146
	s_ashr_i32 s6, s2, 6
	v_lshl_add_u64 v[132:133], v[2:3], 0, v[134:135]
	v_lshl_or_b32 v2, s6, 3, v1
	v_ashrrev_i32_e32 v3, 31, v2
	v_lshlrev_b64 v[2:3], 10, v[2:3]
	v_lshl_add_u64 v[2:3], s[4:5], 0, v[2:3]
	v_lshl_add_u64 v[2:3], v[2:3], 0, v[134:135]
	global_load_dwordx4 v[94:97], v[132:133], off
	global_load_dwordx4 v[86:89], v[132:133], off offset:1024
	global_load_dwordx4 v[54:57], v[132:133], off offset:2048
	global_load_dwordx4 v[42:45], v[132:133], off offset:3072
	global_load_dwordx4 v[98:101], v[2:3], off
	s_movk_i32 s7, 0x1000
	v_add_co_u32_e32 v2, vcc, s7, v132
	s_lshl_b32 s3, s2, 6
	s_nop 0
	v_addc_co_u32_e32 v3, vcc, 0, v133, vcc
	s_movk_i32 s4, 0x2000
	v_add_co_u32_e32 v4, vcc, s4, v132
	s_and_b32 s3, s3, 0xfc0
	s_nop 0
	v_addc_co_u32_e32 v5, vcc, 0, v133, vcc
	s_movk_i32 s4, 0x3000
	s_ashr_i32 s7, s6, 31
	s_lshl_b32 s16, s3, 2
	v_add_co_u32_e32 v4, vcc, s4, v132
	v_and_b32_e32 v106, 7, v0
	s_add_u32 s4, s8, s16
	v_addc_co_u32_e32 v5, vcc, 0, v133, vcc
	s_addc_u32 s5, s9, 0
	v_lshlrev_b32_e32 v2, 5, v106
	v_mov_b32_e32 v3, v135
	v_lshrrev_b32_e32 v107, 3, v0
	v_lshl_add_u64 v[2:3], s[4:5], 0, v[2:3]
	s_lshl_b64 s[4:5], s[6:7], 22
	v_lshl_or_b32 v4, v107, 14, s4
	v_mov_b32_e32 v5, s5
	v_lshl_add_u64 v[2:3], v[2:3], 0, v[4:5]
	s_mov_b64 s[4:5], 0x100000
	v_lshl_add_u64 v[4:5], v[2:3], 0, s[4:5]
	s_mov_b32 s4, 0x100000
	v_add_co_u32_e32 v6, vcc, s4, v2
	s_mov_b64 s[4:5], 0x200000
	s_nop 0
	v_addc_co_u32_e32 v7, vcc, 0, v3, vcc
	global_load_dwordx4 v[26:29], v[2:3], off offset:16
	global_load_dwordx4 v[30:33], v[2:3], off
	global_load_dwordx4 v[22:25], v[6:7], off
	global_load_dwordx4 v[18:21], v[4:5], off offset:16
	v_lshl_add_u64 v[4:5], v[2:3], 0, s[4:5]
	s_mov_b32 s4, 0x200000
	v_add_co_u32_e32 v6, vcc, s4, v2
	s_mov_b64 s[4:5], 0x300000
	s_nop 0
	v_addc_co_u32_e32 v7, vcc, 0, v3, vcc
	v_lshl_add_u64 v[102:103], v[2:3], 0, s[4:5]
	s_mov_b32 s4, 0x300000
	v_add_co_u32_e32 v104, vcc, s4, v2
	global_load_dwordx4 v[14:17], v[6:7], off
	global_load_dwordx4 v[10:13], v[4:5], off offset:16
	v_addc_co_u32_e32 v105, vcc, 0, v3, vcc
	global_load_dwordx4 v[6:9], v[104:105], off
	global_load_dwordx4 v[2:5], v[102:103], off offset:16
	v_lshrrev_b32_e32 v192, 6, v0
	v_bfe_u32 v193, v0, 5, 1
	v_lshlrev_b32_e32 v192, 7, v192
	v_lshl_add_u32 v192, v193, 4, v192
	global_load_dwordx4 v[196:199], v192, s[30:31]
	global_load_dwordx4 v[200:203], v192, s[30:31] offset:32
	global_load_dwordx4 v[204:207], v192, s[30:31] offset:64
	global_load_dwordx4 v[208:211], v192, s[30:31] offset:96
	global_load_dwordx4 v[212:215], v192, s[30:31] offset:1024
	global_load_dwordx4 v[216:219], v192, s[30:31] offset:1056
	global_load_dwordx4 v[220:223], v192, s[30:31] offset:1088
	global_load_dwordx4 v[224:227], v192, s[30:31] offset:1120
	s_mov_b64 s[24:25], 0x1000
	s_mov_b64 s[26:27], 0x2000
	s_mov_b64 s[28:29], 0x3000
	v_lshl_add_u64 v[182:183], v[132:133], 0, s[24:25]
	v_lshl_add_u64 v[184:185], v[132:133], 0, s[26:27]
	v_lshl_add_u64 v[186:187], v[132:133], 0, s[28:29]
	global_load_dwordx4 v[78:81], v[182:183], off offset:1024
	global_load_dwordx4 v[82:85], v[182:183], off offset:2048
	global_load_dwordx4 v[74:77], v[182:183], off offset:3072
	global_load_dwordx4 v[90:93], v[184:185], off offset:-4096
	global_load_dwordx4 v[66:69], v[184:185], off
	global_load_dwordx4 v[70:73], v[184:185], off offset:1024
	global_load_dwordx4 v[62:65], v[184:185], off offset:2048
	global_load_dwordx4 v[58:61], v[184:185], off offset:3072
	global_load_dwordx4 v[50:53], v[186:187], off
	global_load_dwordx4 v[46:49], v[186:187], off offset:1024
	global_load_dwordx4 v[38:41], v[186:187], off offset:2048
	global_load_dwordx4 v[34:37], v[186:187], off offset:3072
	v_mbcnt_lo_u32_b32 v102, -1, 0
	v_mbcnt_hi_u32_b32 v108, -1, v102
	v_and_b32_e32 v102, 64, v108
	v_add_u32_e32 v109, 64, v102
	v_xor_b32_e32 v102, 32, v108
	v_cmp_lt_i32_e32 vcc, v102, v109
	s_load_dwordx2 s[8:9], s[0:1], 0x28
	v_cmp_lt_u32_e64 s[4:5], 31, v146
	v_cndmask_b32_e32 v102, v108, v102, vcc
	v_lshlrev_b32_e32 v105, 2, v102
	v_lshlrev_b32_e32 v130, 5, v1
	s_waitcnt vmcnt(28)
	ds_bpermute_b32 v102, v105, v98
	ds_bpermute_b32 v103, v105, v99
	ds_bpermute_b32 v104, v105, v100
	ds_bpermute_b32 v105, v105, v101
	s_waitcnt lgkmcnt(0)
	v_add_f64 v[98:99], v[98:99], v[102:103]
	v_xor_b32_e32 v102, 16, v108
	v_cmp_lt_i32_e32 vcc, v102, v109
	v_add_f64 v[100:101], v[100:101], v[104:105]
	s_nop 0
	v_cndmask_b32_e32 v102, v108, v102, vcc
	v_lshlrev_b32_e32 v141, 2, v102
	ds_bpermute_b32 v102, v141, v98
	ds_bpermute_b32 v103, v141, v99
	ds_bpermute_b32 v104, v141, v100
	ds_bpermute_b32 v105, v141, v101
	s_waitcnt lgkmcnt(2)
	v_add_f64 v[98:99], v[98:99], v[102:103]
	v_xor_b32_e32 v102, 8, v108
	v_cmp_lt_i32_e32 vcc, v102, v109
	s_waitcnt lgkmcnt(0)
	v_add_f64 v[100:101], v[100:101], v[104:105]
	v_cndmask_b32_e32 v102, v108, v102, vcc
	v_lshlrev_b32_e32 v142, 2, v102
	ds_bpermute_b32 v102, v142, v98
	ds_bpermute_b32 v103, v142, v99
	ds_bpermute_b32 v104, v142, v100
	ds_bpermute_b32 v105, v142, v101
	s_waitcnt lgkmcnt(2)
	v_add_f64 v[98:99], v[98:99], v[102:103]
	v_xor_b32_e32 v102, 4, v108
	v_cmp_lt_i32_e32 vcc, v102, v109
	s_waitcnt lgkmcnt(0)
	v_add_f64 v[100:101], v[100:101], v[104:105]
	v_cndmask_b32_e32 v102, v108, v102, vcc
	v_lshlrev_b32_e32 v143, 2, v102
	ds_bpermute_b32 v102, v143, v98
	ds_bpermute_b32 v103, v143, v99
	ds_bpermute_b32 v104, v143, v100
	ds_bpermute_b32 v105, v143, v101
	s_waitcnt lgkmcnt(2)
	v_add_f64 v[98:99], v[98:99], v[102:103]
	v_xor_b32_e32 v102, 2, v108
	v_cmp_lt_i32_e32 vcc, v102, v109
	s_waitcnt lgkmcnt(0)
	v_add_f64 v[100:101], v[100:101], v[104:105]
	v_cndmask_b32_e32 v102, v108, v102, vcc
	v_lshlrev_b32_e32 v144, 2, v102
	ds_bpermute_b32 v102, v144, v98
	ds_bpermute_b32 v103, v144, v99
	ds_bpermute_b32 v104, v144, v100
	ds_bpermute_b32 v105, v144, v101
	s_waitcnt lgkmcnt(2)
	v_add_f64 v[98:99], v[98:99], v[102:103]
	v_xor_b32_e32 v102, 1, v108
	v_cmp_lt_i32_e32 vcc, v102, v109
	s_waitcnt lgkmcnt(0)
	v_add_f64 v[100:101], v[100:101], v[104:105]
	v_cndmask_b32_e32 v102, v108, v102, vcc
	v_lshlrev_b32_e32 v145, 2, v102
	ds_bpermute_b32 v102, v145, v98
	ds_bpermute_b32 v103, v145, v99
	ds_bpermute_b32 v104, v145, v100
	ds_bpermute_b32 v105, v145, v101
	v_cmp_gt_u32_e32 vcc, 32, v146
	s_and_saveexec_b64 s[10:11], s[4:5]
	s_xor_b64 s[4:5], exec, s[10:11]
	v_lshlrev_b32_e32 v130, 5, v1
	s_or_saveexec_b64 s[10:11], s[4:5]
	s_load_dwordx2 s[14:15], s[0:1], 0x38
	s_xor_b64 exec, exec, s[10:11]
	s_cbranch_execz .LBB1_4
	s_load_dwordx4 s[20:23], s[0:1], 0x8
	v_or_b32_e32 v108, v130, v146
	v_lshlrev_b32_e32 v108, 2, v108
	s_waitcnt lgkmcnt(0)
	v_add_f64 v[98:99], v[98:99], v[102:103]
	s_movk_i32 s12, 0xffef
	s_mov_b32 s4, 0
	v_ldexp_f64 v[98:99], v[98:99], s12
	v_add_f64 v[100:101], v[100:101], v[104:105]
	s_mov_b32 s5, 0x3ee00000
	v_mul_f64 v[102:103], v[98:99], v[98:99]
	v_fma_f64 v[100:101], v[100:101], s[4:5], -v[102:103]
	v_cvt_f32_f64_e32 v100, v[100:101]
	s_mov_b32 s13, 0x800000
	v_add_f32_e32 v100, 0x3727c5ac, v100
	v_mul_f32_e32 v101, 0x4b800000, v100
	v_cmp_gt_f32_e64 s[4:5], s13, v100
	v_cvt_f32_f64_e32 v98, v[98:99]
	s_nop 0
	v_cndmask_b32_e64 v100, v100, v101, s[4:5]
	v_rsq_f32_e32 v100, v100
	v_add_u32_e32 v101, 0, v108
	v_mul_f32_e32 v102, 0x45800000, v100
	v_cndmask_b32_e64 v100, v100, v102, s[4:5]
	v_mul_f32_e32 v100, v100, v190
	v_fma_f32 v98, -v100, v98, v191
	ds_write2st64_b32 v101, v100, v98 offset0:128 offset1:132
.LBB1_4:
	s_or_b64 exec, exec, s[10:11]
	s_waitcnt lgkmcnt(0)
	v_lshrrev_b32_e32 v103, 4, v0
	v_bfe_u32 v104, v0, 3, 2
	v_lshlrev_b32_e32 v102, 4, v0
	v_and_or_b32 v103, v103, 4, v104
	v_lshl_add_u32 v105, v107, 2, 0
	v_lshlrev_b32_e32 v103, 6, v103
	v_and_b32_e32 v102, 48, v102
	s_barrier
	ds_read2st64_b32 v[98:99], v105 offset0:128 offset1:129
	ds_read2st64_b32 v[100:101], v105 offset0:132 offset1:133
	v_add3_u32 v109, 0, v103, v102
	ds_read2st64_b32 v[102:103], v105 offset0:134 offset1:135
	ds_read2st64_b32 v[104:105], v105 offset0:130 offset1:131
	s_movk_i32 s4, 0x70
	v_lshrrev_b32_e32 v108, 5, v146
	s_waitcnt vmcnt(25) lgkmcnt(2)
	v_fma_f32 v22, v22, v99, v101
	v_fma_f32 v23, v23, v99, v101
	s_waitcnt vmcnt(23) lgkmcnt(0)
	v_fma_f32 v14, v14, v104, v102
	v_fma_f32 v15, v15, v104, v102
	v_cvt_pk_bf16_f32 v22, v22, v23
	v_fma_f32 v23, v24, v99, v101
	v_fma_f32 v24, v25, v99, v101
	v_fma_f32 v18, v18, v99, v101
	v_fma_f32 v19, v19, v99, v101
	v_cvt_pk_bf16_f32 v14, v14, v15
	v_fma_f32 v15, v16, v104, v102
	v_fma_f32 v16, v17, v104, v102
	s_waitcnt vmcnt(22)
	v_fma_f32 v10, v10, v104, v102
	v_fma_f32 v11, v11, v104, v102
	s_waitcnt vmcnt(21)
	v_fma_f32 v6, v6, v105, v103
	v_fma_f32 v7, v7, v105, v103
	v_fma_f32 v30, v30, v98, v100
	v_fma_f32 v31, v31, v98, v100
	v_fma_f32 v32, v32, v98, v100
	v_fma_f32 v33, v33, v98, v100
	v_fma_f32 v26, v26, v98, v100
	v_fma_f32 v27, v27, v98, v100
	v_cvt_pk_bf16_f32 v23, v23, v24
	v_cvt_pk_bf16_f32 v24, v18, v19
	v_fma_f32 v18, v20, v99, v101
	v_fmac_f32_e32 v101, v21, v99
	v_cvt_pk_bf16_f32 v15, v15, v16
	v_cvt_pk_bf16_f32 v16, v10, v11
	v_fma_f32 v10, v12, v104, v102
	v_fma_f32 v11, v13, v104, v102
	v_cvt_pk_bf16_f32 v6, v6, v7
	v_fma_f32 v7, v8, v105, v103
	v_fma_f32 v8, v9, v105, v103
	s_waitcnt vmcnt(20)
	v_fma_f32 v2, v2, v105, v103
	v_fma_f32 v3, v3, v105, v103
	v_cvt_pk_bf16_f32 v30, v30, v31
	v_cvt_pk_bf16_f32 v31, v32, v33
	v_cvt_pk_bf16_f32 v32, v26, v27
	v_fma_f32 v26, v28, v98, v100
	v_fma_f32 v27, v29, v98, v100
	v_cvt_pk_bf16_f32 v25, v18, v101
	v_bitop3_b32 v18, v107, s4, 64 bitop3:0xc8
	v_cvt_pk_bf16_f32 v17, v10, v11
	s_movk_i32 s4, 0xb0
	v_mov_b32_e32 v10, 0x80
	v_cvt_pk_bf16_f32 v7, v7, v8
	v_cvt_pk_bf16_f32 v8, v2, v3
	v_fma_f32 v2, v4, v105, v103
	v_fmac_f32_e32 v103, v5, v105
	v_cvt_pk_bf16_f32 v33, v26, v27
	v_lshlrev_b32_e32 v27, 1, v107
	v_bitop3_b32 v10, v107, s4, v10 bitop3:0xc8
	v_cvt_pk_bf16_f32 v9, v2, v103
	s_movk_i32 s4, 0xf0
	v_mov_b32_e32 v2, 0xc0
	v_and_b32_e32 v26, 48, v107
	v_and_b32_e32 v27, 8, v27
	v_bitop3_b32 v2, v107, s4, v2 bitop3:0xc8
	v_or3_b32 v26, v26, v27, v106
	v_or3_b32 v18, v18, v27, v106
	v_or3_b32 v10, v10, v27, v106
	v_or3_b32 v2, v2, v27, v106
	v_lshlrev_b32_e32 v26, 7, v26
	v_lshlrev_b32_e32 v18, 7, v18
	v_lshlrev_b32_e32 v10, 7, v10
	v_lshlrev_b32_e32 v2, 7, v2
	v_and_b32_e32 v26, 0x1e00, v26
	v_and_b32_e32 v18, 0x3e00, v18
	v_and_b32_e32 v10, 0x5e00, v10
	v_and_b32_e32 v2, 0x7e00, v2
	v_add_u32_e32 v26, v109, v26
	v_add_u32_e32 v18, v109, v18
	v_add_u32_e32 v10, v109, v10
	v_add_u32_e32 v2, v109, v2
	v_mov_b32_e32 v131, 0
	ds_write_b128 v26, v[30:33]
	ds_write_b128 v18, v[22:25]
	ds_write_b128 v10, v[14:17]
	ds_write_b128 v2, v[6:9]
	v_lshl_add_u64 v[2:3], v[130:131], 2, s[8:9]
	v_lshlrev_b32_e32 v136, 4, v108
	v_mov_b32_e32 v137, v131
	v_lshl_add_u64 v[138:139], v[2:3], 0, v[136:137]
	s_waitcnt lgkmcnt(0)
	s_barrier
	v_lshlrev_b32_e32 v18, 3, v146
	v_and_b32_e32 v19, 24, v18
	v_and_b32_e32 v20, 0xc0, v134
	v_lshlrev_b32_e32 v21, 1, v0
	v_and_b32_e32 v21, 32, v21
	v_and_b32_e32 v18, 0x100, v18
	v_add3_u32 v19, 0, v19, v20
	v_add3_u32 v140, v19, v21, v18
	ds_read_b64_tr_b16 v[98:99], v140
	ds_read_b64_tr_b16 v[100:101], v140 offset:1024
	ds_read_b64_tr_b16 v[104:105], v140 offset:1536
	ds_read_b64_tr_b16 v[102:103], v140 offset:512
	s_waitcnt vmcnt(0) lgkmcnt(2)
	v_mfma_f32_32x32x16_bf16 v[18:33], v[94:97], v[98:101], v[196:211]
	ds_read_b64_tr_b16 v[98:99], v140 offset:2048
	ds_read_b64_tr_b16 v[100:101], v140 offset:3072
	ds_read_b64_tr_b16 v[108:109], v140 offset:3584
	ds_read_b64_tr_b16 v[106:107], v140 offset:2560
	s_mov_b32 s4, 0x20000
	v_and_b32_e32 v137, 31, v0
	s_waitcnt lgkmcnt(2)
	v_mfma_f32_32x32x16_bf16 v[18:33], v[86:89], v[98:101], v[18:33]
	ds_read_b64_tr_b16 v[98:99], v140 offset:4096
	ds_read_b64_tr_b16 v[100:101], v140 offset:5120
	ds_read_b64_tr_b16 v[112:113], v140 offset:5632
	ds_read_b64_tr_b16 v[110:111], v140 offset:4608
	s_waitcnt lgkmcnt(2)
	v_mfma_f32_32x32x16_bf16 v[18:33], v[54:57], v[98:101], v[18:33]
	v_mfma_f32_32x32x16_bf16 v[2:17], v[94:97], v[102:105], v[196:211]
	ds_read_b64_tr_b16 v[94:95], v140 offset:6144
	ds_read_b64_tr_b16 v[96:97], v140 offset:7168
	ds_read_b64_tr_b16 v[100:101], v140 offset:7680
	ds_read_b64_tr_b16 v[98:99], v140 offset:6656
	s_waitcnt lgkmcnt(2)
	v_mfma_f32_32x32x16_bf16 v[18:33], v[42:45], v[94:97], v[18:33]
	ds_read_b64_tr_b16 v[94:95], v140 offset:8192
	ds_read_b64_tr_b16 v[96:97], v140 offset:9216
	ds_read_b64_tr_b16 v[104:105], v140 offset:9728
	ds_read_b64_tr_b16 v[102:103], v140 offset:8704
	v_mfma_f32_32x32x16_bf16 v[2:17], v[86:89], v[106:109], v[2:17]
	s_waitcnt lgkmcnt(2)
	v_mfma_f32_32x32x16_bf16 v[18:33], v[90:93], v[94:97], v[18:33]
	ds_read_b64_tr_b16 v[86:87], v140 offset:10240
	ds_read_b64_tr_b16 v[88:89], v140 offset:11264
	ds_read_b64_tr_b16 v[96:97], v140 offset:11776
	ds_read_b64_tr_b16 v[94:95], v140 offset:10752
	v_mfma_f32_32x32x16_bf16 v[2:17], v[54:57], v[110:113], v[2:17]
	s_waitcnt lgkmcnt(2)
	v_mfma_f32_32x32x16_bf16 v[18:33], v[78:81], v[86:89], v[18:33]
	ds_read_b64_tr_b16 v[86:87], v140 offset:12288
	ds_read_b64_tr_b16 v[88:89], v140 offset:13312
	ds_read_b64_tr_b16 v[108:109], v140 offset:13824
	ds_read_b64_tr_b16 v[106:107], v140 offset:12800
	v_mfma_f32_32x32x16_bf16 v[2:17], v[42:45], v[98:101], v[2:17]
	s_waitcnt lgkmcnt(2)
	v_mfma_f32_32x32x16_bf16 v[18:33], v[82:85], v[86:89], v[18:33]
	ds_read_b64_tr_b16 v[54:55], v140 offset:14336
	ds_read_b64_tr_b16 v[56:57], v140 offset:15360
	ds_read_b64_tr_b16 v[88:89], v140 offset:15872
	ds_read_b64_tr_b16 v[86:87], v140 offset:14848
	v_mfma_f32_32x32x16_bf16 v[2:17], v[90:93], v[102:105], v[2:17]
	s_waitcnt lgkmcnt(2)
	v_mfma_f32_32x32x16_bf16 v[18:33], v[74:77], v[54:57], v[18:33]
	ds_read_b64_tr_b16 v[54:55], v140 offset:16384
	ds_read_b64_tr_b16 v[56:57], v140 offset:17408
	ds_read_b64_tr_b16 v[112:113], v140 offset:17920
	ds_read_b64_tr_b16 v[110:111], v140 offset:16896
	v_mfma_f32_32x32x16_bf16 v[2:17], v[78:81], v[94:97], v[2:17]
	s_waitcnt lgkmcnt(2)
	v_mfma_f32_32x32x16_bf16 v[18:33], v[66:69], v[54:57], v[18:33]
	ds_read_b64_tr_b16 v[42:43], v140 offset:18432
	ds_read_b64_tr_b16 v[44:45], v140 offset:19456
	ds_read_b64_tr_b16 v[56:57], v140 offset:19968
	ds_read_b64_tr_b16 v[54:55], v140 offset:18944
	v_mfma_f32_32x32x16_bf16 v[2:17], v[82:85], v[106:109], v[2:17]
	s_waitcnt lgkmcnt(2)
	v_mfma_f32_32x32x16_bf16 v[18:33], v[70:73], v[42:45], v[18:33]
	ds_read_b64_tr_b16 v[42:43], v140 offset:20480
	ds_read_b64_tr_b16 v[44:45], v140 offset:21504
	ds_read_b64_tr_b16 v[80:81], v140 offset:22016
	ds_read_b64_tr_b16 v[78:79], v140 offset:20992
	v_mfma_f32_32x32x16_bf16 v[2:17], v[74:77], v[86:89], v[2:17]
	s_waitcnt lgkmcnt(2)
	v_mfma_f32_32x32x16_bf16 v[18:33], v[62:65], v[42:45], v[18:33]
	ds_read_b64_tr_b16 v[42:43], v140 offset:22528
	ds_read_b64_tr_b16 v[44:45], v140 offset:23552
	ds_read_b64_tr_b16 v[76:77], v140 offset:24064
	ds_read_b64_tr_b16 v[74:75], v140 offset:23040
	v_mfma_f32_32x32x16_bf16 v[2:17], v[66:69], v[110:113], v[2:17]
	s_waitcnt lgkmcnt(2)
	v_mfma_f32_32x32x16_bf16 v[18:33], v[58:61], v[42:45], v[18:33]
	v_mfma_f32_32x32x16_bf16 v[2:17], v[70:73], v[54:57], v[2:17]
	ds_read_b64_tr_b16 v[42:43], v140 offset:24576
	ds_read_b64_tr_b16 v[44:45], v140 offset:25600
	ds_read_b64_tr_b16 v[56:57], v140 offset:26112
	ds_read_b64_tr_b16 v[54:55], v140 offset:25088
	s_waitcnt lgkmcnt(2)
	v_mfma_f32_32x32x16_bf16 v[18:33], v[50:53], v[42:45], v[18:33]
	ds_read_b64_tr_b16 v[42:43], v140 offset:26624
	ds_read_b64_tr_b16 v[44:45], v140 offset:27648
	ds_read_b64_tr_b16 v[68:69], v140 offset:28160
	ds_read_b64_tr_b16 v[66:67], v140 offset:27136
	v_mfma_f32_32x32x16_bf16 v[2:17], v[62:65], v[78:81], v[2:17]
	s_waitcnt lgkmcnt(2)
	v_mfma_f32_32x32x16_bf16 v[18:33], v[46:49], v[42:45], v[18:33]
	ds_read_b64_tr_b16 v[42:43], v140 offset:28672
	ds_read_b64_tr_b16 v[44:45], v140 offset:29696
	ds_read_b64_tr_b16 v[150:151], v140 offset:30208
	ds_read_b64_tr_b16 v[148:149], v140 offset:29184
	v_mfma_f32_32x32x16_bf16 v[2:17], v[58:61], v[74:77], v[2:17]
	s_waitcnt lgkmcnt(2)
	v_mfma_f32_32x32x16_bf16 v[18:33], v[38:41], v[42:45], v[18:33]
	v_add_co_u32_e64 v42, s[4:5], s4, v132
	s_nop 1
	v_addc_co_u32_e64 v43, s[4:5], 0, v133, s[4:5]
	s_mov_b32 s4, 0x21000
	s_nop 0
	v_add_co_u32_e64 v44, s[4:5], s4, v132
	v_mfma_f32_32x32x16_bf16 v[2:17], v[50:53], v[54:57], v[2:17]
	s_nop 0
	v_addc_co_u32_e64 v45, s[4:5], 0, v133, s[4:5]
	s_mov_b32 s4, 0x22000
	s_nop 0
	v_add_co_u32_e64 v50, s[4:5], s4, v132
	global_load_dwordx4 v[122:125], v[42:43], off offset:1024
	global_load_dwordx4 v[114:117], v[42:43], off offset:2048
	global_load_dwordx4 v[126:129], v[44:45], off offset:-4096
	global_load_dwordx4 v[110:113], v[44:45], off
	global_load_dwordx4 v[106:109], v[44:45], off offset:1024
	global_load_dwordx4 v[102:105], v[44:45], off offset:2048
	v_addc_co_u32_e64 v51, s[4:5], 0, v133, s[4:5]
	s_mov_b32 s4, 0x23000
	s_nop 0
	v_add_co_u32_e64 v52, s[4:5], s4, v132
	v_mfma_f32_32x32x16_bf16 v[2:17], v[46:49], v[66:69], v[2:17]
	s_nop 0
	v_addc_co_u32_e64 v53, s[4:5], 0, v133, s[4:5]
	global_load_dwordx4 v[98:101], v[44:45], off offset:3072
	global_load_dwordx4 v[94:97], v[52:53], off offset:-4096
	global_load_dwordx4 v[118:121], v[42:43], off offset:3072
	global_load_dwordx4 v[90:93], v[50:51], off offset:1024
	global_load_dwordx4 v[86:89], v[50:51], off offset:2048
	global_load_dwordx4 v[82:85], v[50:51], off offset:3072
	global_load_dwordx4 v[70:73], v[52:53], off
	global_load_dwordx4 v[66:69], v[52:53], off offset:1024
	global_load_dwordx4 v[74:77], v[52:53], off offset:2048
	global_load_dwordx4 v[78:81], v[52:53], off offset:3072
	s_waitcnt lgkmcnt(0)
	v_mfma_f32_32x32x16_bf16 v[2:17], v[38:41], v[148:151], v[2:17]
	ds_read_b64_tr_b16 v[38:39], v140 offset:30720
	ds_read_b64_tr_b16 v[40:41], v140 offset:31744
	ds_read_b64_tr_b16 v[44:45], v140 offset:32256
	ds_read_b64_tr_b16 v[42:43], v140 offset:31232
	s_waitcnt lgkmcnt(0)
	s_barrier
	v_mfma_f32_32x32x16_bf16 v[18:33], v[34:37], v[38:41], v[18:33]
	v_lshl_add_u32 v38, v137, 2, 0
	v_mfma_f32_32x32x16_bf16 v[2:17], v[34:37], v[42:45], v[2:17]
	s_nop 9
	v_max3_f32 v39, |v18|, 0, |v19|
	v_max3_f32 v39, v39, |v20|, |v21|
	v_max3_f32 v39, v39, |v22|, |v23|
	v_max3_f32 v39, v39, |v24|, |v25|
	v_max3_f32 v39, v39, |v26|, |v27|
	v_max3_f32 v39, v39, |v28|, |v29|
	v_max3_f32 v34, v39, |v30|, |v31|
	v_max3_f32 v36, |v2|, 0, |v3|
	v_max3_f32 v36, v36, |v4|, |v5|
	v_max3_f32 v36, v36, |v6|, |v7|
	v_max3_f32 v36, v36, |v8|, |v9|
	v_max3_f32 v36, v36, |v10|, |v11|
	v_max3_f32 v36, v36, |v12|, |v13|
	v_max3_f32 v36, v36, |v14|, |v15|
	v_max3_f32 v34, v34, |v32|, |v33|
	v_max3_f32 v36, v36, |v16|, |v17|
	v_mov_b32_e32 v35, v34
	v_mov_b32_e32 v37, v36
	s_nop 0
	v_permlane32_swap_b32_e32 v34, v35
	v_permlane32_swap_b32_e32 v36, v37
	s_and_saveexec_b64 s[4:5], vcc
	s_cbranch_execz .LBB1_6
	v_max_f32_e32 v34, v34, v34
	v_max_f32_e32 v35, v35, v35
	v_max_f32_e32 v34, v34, v35
	v_and_b32_e32 v35, 0x1c0, v0
	v_max_f32_e32 v36, v36, v36
	v_max_f32_e32 v37, v37, v37
	v_lshl_add_u32 v35, v35, 2, v38
	v_max_f32_e32 v36, v36, v37
	v_add_u32_e32 v35, 0x8800, v35
	ds_write2_b32 v35, v34, v36 offset1:32

.LBB1_10:
	s_or_b64 exec, exec, s[14:15]
	ds_read_b64_tr_b16 v[148:149], v140
	ds_read_b64_tr_b16 v[150:151], v140 offset:1024
	ds_read_b64_tr_b16 v[154:155], v140 offset:1536
	ds_read_b64_tr_b16 v[152:153], v140 offset:512
	v_cmp_eq_u32_e32 vcc, 0, v146
	v_rcp_f32_e32 v138, v147
	s_mov_b32 s4, 0x40000
	s_mov_b32 s20, 0x41000
	s_lshl_b64 s[14:15], s[6:7], 20
	s_lshl_b32 s19, s3, 8
	s_add_u32 s14, s10, s14
	s_mov_b32 s17, 0xc0c0400
	s_mov_b32 s18, 0x4000c0c
	s_waitcnt vmcnt(0) lgkmcnt(2)
	v_mfma_f32_32x32x16_bf16 v[50:65], v[126:129], v[148:151], v[212:227]
	s_waitcnt lgkmcnt(0)
	v_mfma_f32_32x32x16_bf16 v[34:49], v[126:129], v[152:155], v[212:227]
	ds_read_b64_tr_b16 v[126:127], v140 offset:2048
	ds_read_b64_tr_b16 v[128:129], v140 offset:3072
	ds_read_b64_tr_b16 v[150:151], v140 offset:3584
	ds_read_b64_tr_b16 v[148:149], v140 offset:2560
	s_waitcnt lgkmcnt(2)
	v_mfma_f32_32x32x16_bf16 v[50:65], v[122:125], v[126:129], v[50:65]
	s_waitcnt lgkmcnt(0)
	v_mfma_f32_32x32x16_bf16 v[34:49], v[122:125], v[148:151], v[34:49]
	ds_read_b64_tr_b16 v[122:123], v140 offset:4096
	ds_read_b64_tr_b16 v[124:125], v140 offset:5120
	ds_read_b64_tr_b16 v[128:129], v140 offset:5632
	ds_read_b64_tr_b16 v[126:127], v140 offset:4608
	s_waitcnt lgkmcnt(2)
	v_mfma_f32_32x32x16_bf16 v[50:65], v[114:117], v[122:125], v[50:65]
	s_waitcnt lgkmcnt(0)
	v_mfma_f32_32x32x16_bf16 v[34:49], v[114:117], v[126:129], v[34:49]
	ds_read_b64_tr_b16 v[114:115], v140 offset:6144
	ds_read_b64_tr_b16 v[116:117], v140 offset:7168
	ds_read_b64_tr_b16 v[124:125], v140 offset:7680
	ds_read_b64_tr_b16 v[122:123], v140 offset:6656
	v_rcp_f32_e32 v128, v135
	v_lshlrev_b32_e32 v126, 11, v1
	v_mov_b32_e32 v127, 0
	v_mov_b32_e32 v135, v127
	v_mov_b32_e32 v129, 0x4b400000
	s_waitcnt lgkmcnt(2)
	v_mfma_f32_32x32x16_bf16 v[50:65], v[118:121], v[114:117], v[50:65]
	s_waitcnt lgkmcnt(0)
	v_mfma_f32_32x32x16_bf16 v[34:49], v[118:121], v[122:125], v[34:49]
	ds_read_b64_tr_b16 v[114:115], v140 offset:8192
	ds_read_b64_tr_b16 v[116:117], v140 offset:9216
	ds_read_b64_tr_b16 v[120:121], v140 offset:9728
	ds_read_b64_tr_b16 v[118:119], v140 offset:8704
	s_waitcnt lgkmcnt(2)
	v_mfma_f32_32x32x16_bf16 v[50:65], v[110:113], v[114:117], v[50:65]
	s_waitcnt lgkmcnt(0)
	v_mfma_f32_32x32x16_bf16 v[34:49], v[110:113], v[118:121], v[34:49]
	ds_read_b64_tr_b16 v[110:111], v140 offset:10240
	ds_read_b64_tr_b16 v[112:113], v140 offset:11264
	ds_read_b64_tr_b16 v[116:117], v140 offset:11776
	ds_read_b64_tr_b16 v[114:115], v140 offset:10752
	s_waitcnt lgkmcnt(2)
	v_mfma_f32_32x32x16_bf16 v[50:65], v[106:109], v[110:113], v[50:65]
	s_waitcnt lgkmcnt(0)
	v_mfma_f32_32x32x16_bf16 v[34:49], v[106:109], v[114:117], v[34:49]
	ds_read_b64_tr_b16 v[106:107], v140 offset:12288
	ds_read_b64_tr_b16 v[108:109], v140 offset:13312
	ds_read_b64_tr_b16 v[112:113], v140 offset:13824
	ds_read_b64_tr_b16 v[110:111], v140 offset:12800
	s_waitcnt lgkmcnt(2)
	v_mfma_f32_32x32x16_bf16 v[50:65], v[102:105], v[106:109], v[50:65]
	ds_read_b64_tr_b16 v[106:107], v140 offset:14336
	ds_read_b64_tr_b16 v[108:109], v140 offset:15360
	ds_read_b64_tr_b16 v[116:117], v140 offset:15872
	ds_read_b64_tr_b16 v[114:115], v140 offset:14848
	ds_read_b64_tr_b16 v[118:119], v140 offset:16384
	ds_read_b64_tr_b16 v[120:121], v140 offset:17408
	ds_read_b64_tr_b16 v[124:125], v140 offset:17920
	ds_read_b64_tr_b16 v[122:123], v140 offset:16896
	s_waitcnt lgkmcnt(8)
	v_mfma_f32_32x32x16_bf16 v[34:49], v[102:105], v[110:113], v[34:49]
	s_waitcnt lgkmcnt(6)
	v_mfma_f32_32x32x16_bf16 v[50:65], v[98:101], v[106:109], v[50:65]
	ds_read_b64_tr_b16 v[102:103], v140 offset:18432
	ds_read_b64_tr_b16 v[104:105], v140 offset:19456
	ds_read_b64_tr_b16 v[108:109], v140 offset:19968
	ds_read_b64_tr_b16 v[106:107], v140 offset:18944
	s_waitcnt lgkmcnt(8)
	v_mfma_f32_32x32x16_bf16 v[34:49], v[98:101], v[114:117], v[34:49]
	ds_read_b64_tr_b16 v[98:99], v140 offset:20480
	ds_read_b64_tr_b16 v[100:101], v140 offset:21504
	ds_read_b64_tr_b16 v[112:113], v140 offset:22016
	ds_read_b64_tr_b16 v[110:111], v140 offset:20992
	ds_read_b64_tr_b16 v[146:147], v140 offset:22528
	ds_read_b64_tr_b16 v[148:149], v140 offset:23552
	ds_read_b64_tr_b16 v[152:153], v140 offset:24064
	ds_read_b64_tr_b16 v[150:151], v140 offset:23040
	s_waitcnt lgkmcnt(14)
	v_mfma_f32_32x32x16_bf16 v[50:65], v[94:97], v[118:121], v[50:65]
	ds_read_b64_tr_b16 v[118:119], v140 offset:24576
	ds_read_b64_tr_b16 v[120:121], v140 offset:25600
	ds_read_b64_tr_b16 v[156:157], v140 offset:26112
	ds_read_b64_tr_b16 v[154:155], v140 offset:25088
	ds_read_b64_tr_b16 v[158:159], v140 offset:26624
	ds_read_b64_tr_b16 v[160:161], v140 offset:27648
	ds_read_b64_tr_b16 v[164:165], v140 offset:28160
	ds_read_b64_tr_b16 v[162:163], v140 offset:27136
	ds_read_b64_tr_b16 v[166:167], v140 offset:28672
	ds_read_b64_tr_b16 v[168:169], v140 offset:29696
	ds_read_b64_tr_b16 v[172:173], v140 offset:30208
	ds_read_b64_tr_b16 v[170:171], v140 offset:29184
	ds_read_b64_tr_b16 v[174:175], v140 offset:30720
	ds_read_b64_tr_b16 v[176:177], v140 offset:31744
	ds_read_b64_tr_b16 v[180:181], v140 offset:32256
	ds_read_b64_tr_b16 v[178:179], v140 offset:31232
	s_waitcnt lgkmcnt(14)
	v_mfma_f32_32x32x16_bf16 v[34:49], v[94:97], v[122:125], v[34:49]
	v_mul_f32_e32 v94, 0x42fe0000, v128
	v_mul_f32_e32 v94, 0x3f7fffff, v94
	v_fmaak_f32 v97, v23, v94, 0x4b400000
	v_fmaak_f32 v95, v19, v94, 0x4b400000
	v_fmaak_f32 v96, v18, v94, 0x4b400000
	v_fmaak_f32 v21, v21, v94, 0x4b400000
	v_fmaak_f32 v20, v20, v94, 0x4b400000
	v_mfma_f32_32x32x16_bf16 v[50:65], v[90:93], v[102:105], v[50:65]
	v_fmaak_f32 v102, v22, v94, 0x4b400000
	v_add_co_u32_e64 v22, s[4:5], s4, v132
	v_fmaak_f32 v104, v24, v94, 0x4b400000
	s_nop 0
	v_addc_co_u32_e64 v23, s[4:5], 0, v133, s[4:5]
	v_add_co_u32_e64 v24, s[4:5], s20, v132
	v_mfma_f32_32x32x16_bf16 v[34:49], v[90:93], v[106:109], v[34:49]
	v_fmaak_f32 v103, v25, v94, 0x4b400000
	v_addc_co_u32_e64 v25, s[4:5], 0, v133, s[4:5]
	s_addc_u32 s5, s11, s15
	s_add_u32 s4, s14, s19
	s_addc_u32 s5, s5, 0
	v_lshl_add_u64 v[18:19], s[4:5], 0, v[126:127]
	v_mfma_f32_32x32x16_bf16 v[50:65], v[86:89], v[98:101], v[50:65]
	v_fmaak_f32 v27, v27, v94, 0x4b400000
	v_fmaak_f32 v26, v26, v94, 0x4b400000
	v_fmaak_f32 v29, v29, v94, 0x4b400000
	v_fmaak_f32 v28, v28, v94, 0x4b400000
	v_fmaak_f32 v31, v31, v94, 0x4b400000
	v_fmaak_f32 v30, v30, v94, 0x4b400000
	v_fmaak_f32 v98, v33, v94, 0x4b400000
	v_mfma_f32_32x32x16_bf16 v[34:49], v[86:89], v[110:113], v[34:49]
	v_fmaak_f32 v94, v32, v94, 0x4b400000
	v_lshl_add_u64 v[32:33], v[18:19], 0, v[134:135]
	v_perm_b32 v18, v95, v96, s17
	v_perm_b32 v19, v21, v20, s18
	v_perm_b32 v20, v97, v102, s17
	v_perm_b32 v21, v103, v104, s18
	v_or_b32_e32 v18, v18, v19
	v_mfma_f32_32x32x16_bf16 v[50:65], v[82:85], v[146:149], v[50:65]
	v_or_b32_e32 v19, v20, v21
	v_mul_f32_e32 v20, 0x42fe0000, v138
	v_mul_f32_e32 v126, 0x3f7fffff, v20
	s_mov_b32 s4, 0x42000
	v_perm_b32 v21, v31, v30, s17
	v_fmaak_f32 v128, v3, v126, 0x4b400000
	v_perm_b32 v3, v98, v94, s18
	v_mfma_f32_32x32x16_bf16 v[34:49], v[82:85], v[150:153], v[34:49]
	v_fmaak_f32 v134, v2, v126, 0x4b400000
	v_add_co_u32_e64 v2, s[4:5], s4, v132
	v_perm_b32 v26, v27, v26, s17
	v_perm_b32 v27, v29, v28, s18
	v_or_b32_e32 v21, v21, v3
	v_addc_co_u32_e64 v3, s[4:5], 0, v133, s[4:5]
	v_mfma_f32_32x32x16_bf16 v[50:65], v[70:73], v[118:121], v[50:65]
	v_or_b32_e32 v20, v26, v27
	s_mov_b32 s4, 0x43000
	global_load_dwordx4 v[114:117], v[22:23], off offset:1024
	global_load_dwordx4 v[110:113], v[22:23], off offset:2048
	global_load_dwordx4 v[118:121], v[24:25], off offset:-4096
	global_load_dwordx4 v[102:105], v[24:25], off
	v_fmaak_f32 v5, v5, v126, 0x4b400000
	global_store_dwordx4 v[32:33], v[18:21], off
	global_load_dwordx4 v[94:97], v[24:25], off offset:1024
	global_load_dwordx4 v[82:85], v[24:25], off offset:2048
	s_waitcnt lgkmcnt(12)
	v_mfma_f32_32x32x16_bf16 v[34:49], v[70:73], v[154:157], v[34:49]
	v_add_co_u32_e64 v18, s[4:5], s4, v132
	v_fmaak_f32 v4, v4, v126, 0x4b400000
	s_nop 0
	v_addc_co_u32_e64 v19, s[4:5], 0, v133, s[4:5]
	global_load_dwordx4 v[90:93], v[24:25], off offset:3072
	global_load_dwordx4 v[106:109], v[18:19], off offset:-4096
	global_load_dwordx4 v[122:125], v[22:23], off offset:3072
	global_load_dwordx4 v[98:101], v[2:3], off offset:1024
	global_load_dwordx4 v[86:89], v[2:3], off offset:2048
	global_load_dwordx4 v[70:73], v[2:3], off offset:3072
	v_fmaak_f32 v3, v8, v126, 0x4b400000
	s_waitcnt lgkmcnt(10)
	v_mfma_f32_32x32x16_bf16 v[50:65], v[66:69], v[158:161], v[50:65]
	v_fmaak_f32 v8, v11, v126, 0x4b400000
	v_fmaak_f32 v11, v12, v126, 0x4b400000
	v_fmaak_f32 v2, v9, v126, 0x4b400000
	v_fmaak_f32 v9, v10, v126, 0x4b400000
	v_fmaak_f32 v10, v13, v126, 0x4b400000
	v_fmaak_f32 v7, v7, v126, 0x4b400000
	v_fmaak_f32 v6, v6, v126, 0x4b400000
	s_waitcnt lgkmcnt(8)
	v_mfma_f32_32x32x16_bf16 v[34:49], v[66:69], v[162:165], v[34:49]
	global_load_dwordx4 v[28:31], v[18:19], off
	global_load_dwordx4 v[66:69], v[18:19], off offset:1024
	global_load_dwordx4 v[24:27], v[18:19], off offset:2048
	s_nop 0
	global_load_dwordx4 v[18:21], v[18:19], off offset:3072
	v_perm_b32 v4, v5, v4, s18
	v_perm_b32 v5, v7, v6, s17
	v_perm_b32 v2, v2, v3, s18
	v_or_b32_e32 v5, v5, v2
	v_perm_b32 v2, v8, v9, s17
	v_fmaak_f32 v15, v15, v126, 0x4b400000
	s_waitcnt lgkmcnt(4)
	v_mfma_f32_32x32x16_bf16 v[34:49], v[74:77], v[170:173], v[34:49]
	v_fmaak_f32 v14, v14, v126, 0x4b400000
	v_fmac_f32_e32 v129, v16, v126
	v_fmaak_f32 v16, v17, v126, 0x4b400000
	v_perm_b32 v3, v10, v11, s18
	v_perm_b32 v17, v128, v134, s17
	v_or_b32_e32 v4, v17, v4
	v_mfma_f32_32x32x16_bf16 v[50:65], v[74:77], v[166:169], v[50:65]
	s_waitcnt lgkmcnt(0)
	v_mfma_f32_32x32x16_bf16 v[34:49], v[78:81], v[178:181], v[34:49]
	v_mfma_f32_32x32x16_bf16 v[50:65], v[78:81], v[174:177], v[50:65]
	s_nop 10
	v_max3_f32 v22, |v34|, 0, |v35|
	v_max3_f32 v22, v22, |v36|, |v37|
	v_max3_f32 v22, v22, |v38|, |v39|
	v_max3_f32 v22, v22, |v40|, |v41|
	v_max3_f32 v22, v22, |v42|, |v43|
	v_max3_f32 v22, v22, |v44|, |v45|
	v_max3_f32 v22, v22, |v46|, |v47|
	v_max3_f32 v12, |v50|, 0, |v51|
	v_max3_f32 v12, v12, |v52|, |v53|
	v_max3_f32 v12, v12, |v54|, |v55|
	v_max3_f32 v12, v12, |v56|, |v57|
	v_max3_f32 v12, v12, |v58|, |v59|
	v_max3_f32 v12, v12, |v60|, |v61|
	v_max3_f32 v22, v22, |v48|, |v49|
	v_max3_f32 v12, v12, |v62|, |v63|
	v_mov_b32_e32 v23, v22
	v_max3_f32 v12, v12, |v64|, |v65|
	s_nop 0
	v_permlane32_swap_b32_e32 v22, v23
	v_mov_b32_e32 v13, v12
	v_max_f32_e32 v23, v23, v23
	v_max_f32_e32 v22, v22, v22
	v_permlane32_swap_b32_e32 v12, v13
	v_max_f32_e32 v22, v22, v23
	v_max3_f32 v12, v12, v13, v22
	v_or_b32_e32 v6, v2, v3
	v_perm_b32 v2, v15, v14, s17
	v_perm_b32 v3, v16, v129, s18
	v_or_b32_e32 v7, v2, v3
	global_store_dwordx4 v[32:33], v[4:7], off offset:1024
	v_max_f32_dpp v12, v12, v12 quad_perm:[1,0,3,2] row_mask:0xf bank_mask:0xf
	s_nop 1
	v_max_f32_dpp v12, v12, v12 quad_perm:[2,3,0,1] row_mask:0xf bank_mask:0xf
	s_nop 1
	v_max_f32_dpp v12, v12, v12 row_half_mirror row_mask:0xf bank_mask:0xf
	s_nop 1
	v_max_f32_dpp v12, v12, v12 row_mirror row_mask:0xf bank_mask:0xf
	v_mov_b32_e32 v13, v12
	s_nop 1
	v_permlane16_swap_b32_e32 v13, v12
	v_max_f32_e32 v2, v13, v12
	s_waitcnt lgkmcnt(0)
	s_barrier
	s_and_saveexec_b64 s[4:5], vcc
	v_lshl_add_u32 v1, v1, 2, 0
	ds_write_b32 v1, v2 offset:34816
	s_or_b64 exec, exec, s[4:5]
	s_waitcnt lgkmcnt(0)
	s_barrier
	ds_read_b128 v[2:5], v127 offset:34816
	ds_read_b128 v[6:9], v127 offset:34832
	s_mov_b32 s4, 0x1e3ce508
	v_cmp_eq_u32_e32 vcc, 0, v0
	s_waitcnt lgkmcnt(1)
	v_max_f32_e32 v1, v2, v2
	v_max_f32_e32 v1, 0, v1
	v_max3_f32 v1, v1, v3, v4
	s_waitcnt lgkmcnt(0)
	v_max3_f32 v1, v1, v5, v6
	v_max3_f32 v1, v1, v7, v8
	v_max3_f32 v1, v1, v9, s4
	s_and_saveexec_b64 s[4:5], vcc
	s_cbranch_execz .LBB1_14
	s_load_dwordx2 s[0:1], s[0:1], 0x40
	s_andn2_b32 s2, s2, 63
	s_lshr_b32 s14, s3, 6
	s_or_b32 s14, s14, s2
	s_ashr_i32 s15, s14, 31
	s_lshl_b64 s[14:15], s[14:15], 2
	s_waitcnt lgkmcnt(0)
	s_add_u32 s0, s0, s14
	s_addc_u32 s1, s1, s15
	v_mov_b32_e32 v2, 0
	v_mul_f32_e32 v3, 0x3c010204, v1
	global_store_dword v2, v3, s[0:1]

	.amdhsa_kernel _Z10qkv_kernelPKfS0_S0_PKdPKtS0_PhPfS6_
		.amdhsa_group_segment_fixed_size 0
		.amdhsa_private_segment_fixed_size 0
		.amdhsa_kernarg_size 72
		.amdhsa_user_sgpr_count 2
		.amdhsa_user_sgpr_dispatch_ptr 0
		.amdhsa_user_sgpr_queue_ptr 0
		.amdhsa_user_sgpr_kernarg_segment_ptr 1
		.amdhsa_user_sgpr_dispatch_id 0
		.amdhsa_user_sgpr_kernarg_preload_length 0
		.amdhsa_user_sgpr_kernarg_preload_offset 0
		.amdhsa_user_sgpr_private_segment_size 0
		.amdhsa_uses_dynamic_stack 0
		.amdhsa_enable_private_segment 0
		.amdhsa_system_sgpr_workgroup_id_x 1
		.amdhsa_system_sgpr_workgroup_id_y 0
		.amdhsa_system_sgpr_workgroup_id_z 0
		.amdhsa_system_sgpr_workgroup_info 0
		.amdhsa_system_vgpr_workitem_id 0
		.amdhsa_next_free_vgpr 228
		.amdhsa_next_free_sgpr 32
		.amdhsa_accum_offset 228
		.amdhsa_reserve_vcc 1
		.amdhsa_float_round_mode_32 0
		.amdhsa_float_round_mode_16_64 0
		.amdhsa_float_denorm_mode_32 3
		.amdhsa_float_denorm_mode_16_64 3
		.amdhsa_dx10_clamp 1
		.amdhsa_ieee_mode 1
		.amdhsa_fp16_overflow 0
		.amdhsa_tg_split 0
		.amdhsa_exception_fp_ieee_invalid_op 0
		.amdhsa_exception_fp_denorm_src 0
		.amdhsa_exception_fp_ieee_div_zero 0
		.amdhsa_exception_fp_ieee_overflow 0
		.amdhsa_exception_fp_ieee_underflow 0
		.amdhsa_exception_fp_ieee_inexact 0
		.amdhsa_exception_int_div_zero 0
	.end_amdhsa_kernel

amdhsa.kernels:
  - .agpr_count:     0
    .args:
      - .actual_access:  read_only
        .address_space:  global
        .offset:         0
        .size:           8
        .value_kind:     global_buffer
      - .actual_access:  read_only
        .address_space:  global
        .offset:         8
        .size:           8
        .value_kind:     global_buffer
      - .actual_access:  read_only
        .address_space:  global
        .offset:         16
        .size:           8
        .value_kind:     global_buffer
      - .actual_access:  write_only
        .address_space:  global
        .offset:         24
        .size:           8
        .value_kind:     global_buffer
      - .actual_access:  write_only
        .address_space:  global
        .offset:         32
        .size:           8
        .value_kind:     global_buffer
      - .actual_access:  write_only
        .address_space:  global
        .offset:         40
        .size:           8
        .value_kind:     global_buffer
    .group_segment_fixed_size: 512
    .kernarg_segment_align: 8
    .kernarg_segment_size: 48
    .language:       OpenCL C
    .language_version:
      - 2
      - 0
    .max_flat_workgroup_size: 1024
    .name:           _Z11prep_kernelPKfS0_S0_PdPtS2_
    .private_segment_fixed_size: 0
    .sgpr_count:     26
    .sgpr_spill_count: 0
    .symbol:         _Z11prep_kernelPKfS0_S0_PdPtS2_.kd
    .uniform_work_group_size: 1
    .uses_dynamic_stack: false
    .vgpr_count:     32
    .vgpr_spill_count: 0
    .wavefront_size: 64
  - .agpr_count:     0
    .args:
      - .actual_access:  read_only
        .address_space:  global
        .offset:         0
        .size:           8
        .value_kind:     global_buffer
      - .actual_access:  read_only
        .address_space:  global
        .offset:         8
        .size:           8
        .value_kind:     global_buffer
      - .actual_access:  read_only
        .address_space:  global
        .offset:         16
        .size:           8
        .value_kind:     global_buffer
      - .actual_access:  read_only
        .address_space:  global
        .offset:         24
        .size:           8
        .value_kind:     global_buffer
      - .actual_access:  read_only
        .address_space:  global
        .offset:         32
        .size:           8
        .value_kind:     global_buffer
      - .actual_access:  read_only
        .address_space:  global
        .offset:         40
        .size:           8
        .value_kind:     global_buffer
      - .actual_access:  write_only
        .address_space:  global
        .offset:         48
        .size:           8
        .value_kind:     global_buffer
      - .actual_access:  write_only
        .address_space:  global
        .offset:         56
        .size:           8
        .value_kind:     global_buffer
      - .actual_access:  write_only
        .address_space:  global
        .offset:         64
        .size:           8
        .value_kind:     global_buffer
    .group_segment_fixed_size: 0
    .kernarg_segment_align: 8
    .kernarg_segment_size: 72
    .language:       OpenCL C
    .language_version:
      - 2
      - 0
    .max_flat_workgroup_size: 512
    .name:           _Z10qkv_kernelPKfS0_S0_PKdPKtS0_PhPfS6_
    .private_segment_fixed_size: 0
    .sgpr_count:     38
    .sgpr_spill_count: 0
    .symbol:         _Z10qkv_kernelPKfS0_S0_PKdPKtS0_PhPfS6_.kd
    .uniform_work_group_size: 1
    .uses_dynamic_stack: false
    .vgpr_count:     228
    .vgpr_spill_count: 0
    .wavefront_size: 64
  - .agpr_count:     0
    .args:
      - .actual_access:  read_only
        .address_space:  global
        .offset:         0
        .size:           8
        .value_kind:     global_buffer
      - .address_space:  global
        .offset:         8
        .size:           8
        .value_kind:     global_buffer
      - .address_space:  global
        .offset:         16
        .size:           8
        .value_kind:     global_buffer
      - .actual_access:  read_only
        .address_space:  global
        .offset:         24
        .size:           8
        .value_kind:     global_buffer
      - .actual_access:  read_only
        .address_space:  global
        .offset:         32
        .size:           8
        .value_kind:     global_buffer
      - .actual_access:  write_only
        .address_space:  global
        .offset:         40
        .size:           8
        .value_kind:     global_buffer
      - .actual_access:  write_only
        .address_space:  global
        .offset:         48
        .size:           8
        .value_kind:     global_buffer
      - .actual_access:  write_only
        .address_space:  global
        .offset:         56
        .size:           8
        .value_kind:     global_buffer
    .group_segment_fixed_size: 0
    .kernarg_segment_align: 8
    .kernarg_segment_size: 64
    .language:       OpenCL C
    .language_version:
      - 2
      - 0
    .max_flat_workgroup_size: 512
    .name:           _Z11attn_kernelPKhS0_S0_PKfS2_PhPfS4_
    .private_segment_fixed_size: 0
    .sgpr_count:     72
    .sgpr_spill_count: 0
    .symbol:         _Z11attn_kernelPKhS0_S0_PKfS2_PhPfS4_.kd
    .uniform_work_group_size: 1
    .uses_dynamic_stack: false
    .vgpr_count:     256
    .vgpr_spill_count: 0
    .wavefront_size: 64
  - .agpr_count:     0
    .args:
      - .actual_access:  read_only
        .address_space:  global
        .offset:         0
        .size:           8
        .value_kind:     global_buffer
      - .actual_access:  read_only
        .address_space:  global
        .offset:         8
        .size:           8
        .value_kind:     global_buffer
      - .actual_access:  read_only
        .address_space:  global
        .offset:         16
        .size:           8
        .value_kind:     global_buffer
      - .actual_access:  read_only
        .address_space:  global
        .offset:         24
        .size:           8
        .value_kind:     global_buffer
      - .actual_access:  read_only
        .address_space:  global
        .offset:         32
        .size:           8
        .value_kind:     global_buffer
      - .actual_access:  read_only
        .address_space:  global
        .offset:         40
        .size:           8
        .value_kind:     global_buffer
      - .actual_access:  write_only
        .address_space:  global
        .offset:         48
        .size:           8
        .value_kind:     global_buffer
    .group_segment_fixed_size: 16640
    .kernarg_segment_align: 8
    .kernarg_segment_size: 56
    .language:       OpenCL C
    .language_version:
      - 2
      - 0
    .max_flat_workgroup_size: 512
    .name:           _Z14outproj_kernelPKhPKfS2_PKtS2_S2_Pf
    .private_segment_fixed_size: 0
    .sgpr_count:     26
    .sgpr_spill_count: 0
    .symbol:         _Z14outproj_kernelPKhPKfS2_PKtS2_S2_Pf.kd
    .uniform_work_group_size: 1
    .uses_dynamic_stack: false
    .vgpr_count:     109
    .vgpr_spill_count: 0
    .wavefront_size: 64
